# grand stack plus residual-epilogue row partial sums: xor-16 LDS swizzle replaced by a permlane16 swap (24 sites)
# speedup vs baseline: 1.0113x; 1.0006x over previous
; __device__ __forceinline__ void st_wt4(void* p, float v) { asm volatile("global_store_dword %0, %1, off sc1" :: "v"(p), "v"(v) : "memory"); }
; template <int M> __device__ __forceinline__ float xor_add(float v) {
;     if constexpr (M < 32) return v + __int_as_float(__builtin_amdgcn_ds_swizzle(__float_as_int(v), (M << 10) | 0x1f));
;     else { auto rr = __builtin_amdgcn_permlane32_swap(__float_as_uint(v), __float_as_uint(v), false, false); return __uint_as_float(rr[0]) + __uint_as_float(rr[1]); }
;     __device__ __forceinline__ void operator()(const f32x4 (&acc)[2][2][4][2], const Unit& u, int wr, int wc, int fr, int fq) const {
;     ...
;                     ss += ((h0[0] * h0[0] + h0[1] * h0[1]) + (h0[2] * h0[2] + h0[3] * h0[3])) + ((h1[0] * h1[0] + h1[1] * h1[1]) + (h1[2] * h1[2] + h1[3] * h1[3]));
;                 }
;                 ss = xor_add<16>(ss); ss = xor_add<32>(ss);
;                 if (fq == 0) { if (WT && wt) st_wt4(ssqp + SO + (size_t)row * 16 + u.pn * 4 + wc, ss); else ssqp[SO + (size_t)row * 16 + u.pn * 4 + wc] = ss; }
.LBB0_762:
	s_nop 0
	v_mul_f32_e32 v114, v189, v189
	v_mul_f32_e32 v115, v185, v185
	v_fmac_f32_e32 v114, v188, v188
	v_fmac_f32_e32 v115, v184, v184
	v_add_f32_e32 v114, v114, v115
	v_mul_f32_e32 v115, v129, v129
	v_mul_f32_e32 v116, v127, v127
	v_fmac_f32_e32 v115, v128, v128
	v_fmac_f32_e32 v116, v126, v126
	v_add_f32_e32 v115, v115, v116
	v_add_f32_e32 v114, v114, v115
	v_mul_f32_e32 v115, v123, v123
	v_mul_f32_e32 v116, v121, v121
	v_fmac_f32_e32 v115, v122, v122
	v_fmac_f32_e32 v116, v120, v120
	v_add_f32_e32 v115, v115, v116
	v_mul_f32_e32 v116, v125, v125
	v_mul_f32_e32 v117, v119, v119
	v_fmac_f32_e32 v116, v124, v124
	v_fmac_f32_e32 v117, v118, v118
	v_add_f32_e32 v116, v116, v117
	v_add_f32_e32 v115, v115, v116
	v_add_f32_e32 v114, v114, v115
	v_mov_b32_e32 v115, v114
	s_nop 1
	v_permlane16_swap_b32_e32 v114, v115
	s_lshl_b32 s28, s28, 2
	v_cmp_eq_u32_e64 s[6:7], 0, v195
	s_ashr_i32 s29, s28, 31
	s_waitcnt lgkmcnt(0)
	v_add_f32_e32 v114, v114, v115
	v_mov_b32_e32 v115, v114
	s_nop 1
	v_permlane32_swap_b32_e32 v114, v115
	s_and_saveexec_b64 s[30:31], s[6:7]
	s_cbranch_execz .LBB0_766
	v_add_f32_e32 v116, v114, v115
	v_lshlrev_b64 v[114:115], 6, v[168:169]
	v_lshl_add_u64 v[114:115], s[10:11], 0, v[114:115]
	v_lshl_add_u64 v[114:115], s[28:29], 2, v[114:115]
	s_lshl_b32 s50, s46, 2
	v_lshl_add_u64 v[114:115], v[114:115], 0, s[50:51]
	s_and_b64 vcc, exec, s[12:13]
	s_cbranch_vccz .LBB0_858
	global_store_dword v[114:115], v116, off
	s_cbranch_execnz .LBB0_766

; __device__ __forceinline__ void st_wt4(void* p, float v) { asm volatile("global_store_dword %0, %1, off sc1" :: "v"(p), "v"(v) : "memory"); }
; template <int M> __device__ __forceinline__ float xor_add(float v) {
;     if constexpr (M < 32) return v + __int_as_float(__builtin_amdgcn_ds_swizzle(__float_as_int(v), (M << 10) | 0x1f));
;     else { auto rr = __builtin_amdgcn_permlane32_swap(__float_as_uint(v), __float_as_uint(v), false, false); return __uint_as_float(rr[0]) + __uint_as_float(rr[1]); }
;     __device__ __forceinline__ void operator()(const f32x4 (&acc)[2][2][4][2], const Unit& u, int wr, int wc, int fr, int fq) const {
;     ...
;                     ss += ((h0[0] * h0[0] + h0[1] * h0[1]) + (h0[2] * h0[2] + h0[3] * h0[3])) + ((h1[0] * h1[0] + h1[1] * h1[1]) + (h1[2] * h1[2] + h1[3] * h1[3]));
;                 }
;                 ss = xor_add<16>(ss); ss = xor_add<32>(ss);
;                 if (fq == 0) { if (WT && wt) st_wt4(ssqp + SO + (size_t)row * 16 + u.pn * 4 + wc, ss); else ssqp[SO + (size_t)row * 16 + u.pn * 4 + wc] = ss; }
.LBB0_772:
	s_nop 0
	v_mul_f32_e32 v98, v115, v115
	v_mul_f32_e32 v99, v113, v113
	v_fmac_f32_e32 v98, v114, v114
	v_fmac_f32_e32 v99, v112, v112
	v_add_f32_e32 v98, v98, v99
	v_mul_f32_e32 v99, v117, v117
	v_mul_f32_e32 v100, v111, v111
	v_fmac_f32_e32 v99, v116, v116
	v_fmac_f32_e32 v100, v110, v110
	v_add_f32_e32 v99, v99, v100
	v_add_f32_e32 v98, v98, v99
	v_mul_f32_e32 v99, v107, v107
	v_mul_f32_e32 v100, v105, v105
	v_fmac_f32_e32 v99, v106, v106
	v_fmac_f32_e32 v100, v104, v104
	v_add_f32_e32 v99, v99, v100
	v_mul_f32_e32 v100, v109, v109
	v_mul_f32_e32 v101, v103, v103
	v_fmac_f32_e32 v100, v108, v108
	v_fmac_f32_e32 v101, v102, v102
	v_add_f32_e32 v100, v100, v101
	v_add_f32_e32 v99, v99, v100
	v_add_f32_e32 v98, v98, v99
	v_mov_b32_e32 v99, v98
	s_nop 1
	v_permlane16_swap_b32_e32 v98, v99
	s_waitcnt lgkmcnt(0)
	v_add_f32_e32 v98, v98, v99
	v_mov_b32_e32 v99, v98
	s_nop 1
	v_permlane32_swap_b32_e32 v98, v99
	s_and_saveexec_b64 s[30:31], s[6:7]
	s_cbranch_execz .LBB0_776
	v_add_f32_e32 v100, v98, v99
	v_lshlrev_b64 v[98:99], 6, v[180:181]
	v_lshl_add_u64 v[98:99], s[10:11], 0, v[98:99]
	v_lshl_add_u64 v[98:99], s[28:29], 2, v[98:99]
	s_lshl_b32 s50, s46, 2
	s_and_b64 vcc, exec, s[4:5]
	v_lshl_add_u64 v[98:99], v[98:99], 0, s[50:51]
	s_cbranch_vccnz .LBB0_859
	global_store_dword v[98:99], v100, off
	s_cbranch_execnz .LBB0_776

; __device__ __forceinline__ void st_wt4(void* p, float v) { asm volatile("global_store_dword %0, %1, off sc1" :: "v"(p), "v"(v) : "memory"); }
; template <int M> __device__ __forceinline__ float xor_add(float v) {
;     if constexpr (M < 32) return v + __int_as_float(__builtin_amdgcn_ds_swizzle(__float_as_int(v), (M << 10) | 0x1f));
;     else { auto rr = __builtin_amdgcn_permlane32_swap(__float_as_uint(v), __float_as_uint(v), false, false); return __uint_as_float(rr[0]) + __uint_as_float(rr[1]); }
;     __device__ __forceinline__ void operator()(const f32x4 (&acc)[2][2][4][2], const Unit& u, int wr, int wc, int fr, int fq) const {
;     ...
;                     ss += ((h0[0] * h0[0] + h0[1] * h0[1]) + (h0[2] * h0[2] + h0[3] * h0[3])) + ((h1[0] * h1[0] + h1[1] * h1[1]) + (h1[2] * h1[2] + h1[3] * h1[3]));
;                 }
;                 ss = xor_add<16>(ss); ss = xor_add<32>(ss);
;                 if (fq == 0) { if (WT && wt) st_wt4(ssqp + SO + (size_t)row * 16 + u.pn * 4 + wc, ss); else ssqp[SO + (size_t)row * 16 + u.pn * 4 + wc] = ss; }
.LBB0_782:
	s_nop 0
	v_mul_f32_e32 v82, v99, v99
	v_mul_f32_e32 v83, v97, v97
	v_fmac_f32_e32 v82, v98, v98
	v_fmac_f32_e32 v83, v96, v96
	v_add_f32_e32 v82, v82, v83
	v_mul_f32_e32 v83, v101, v101
	v_mul_f32_e32 v84, v95, v95
	v_fmac_f32_e32 v83, v100, v100
	v_fmac_f32_e32 v84, v94, v94
	v_add_f32_e32 v83, v83, v84
	v_add_f32_e32 v82, v82, v83
	v_mul_f32_e32 v83, v91, v91
	v_mul_f32_e32 v84, v89, v89
	v_fmac_f32_e32 v83, v90, v90
	v_fmac_f32_e32 v84, v88, v88
	v_add_f32_e32 v83, v83, v84
	v_mul_f32_e32 v84, v93, v93
	v_mul_f32_e32 v85, v87, v87
	v_fmac_f32_e32 v84, v92, v92
	v_fmac_f32_e32 v85, v86, v86
	v_add_f32_e32 v84, v84, v85
	v_add_f32_e32 v83, v83, v84
	v_add_f32_e32 v82, v82, v83
	v_mov_b32_e32 v83, v82
	s_nop 1
	v_permlane16_swap_b32_e32 v82, v83
	s_waitcnt lgkmcnt(0)
	v_add_f32_e32 v82, v82, v83
	v_mov_b32_e32 v83, v82
	s_nop 1
	v_permlane32_swap_b32_e32 v82, v83
	s_and_saveexec_b64 s[30:31], s[6:7]
	s_cbranch_execz .LBB0_786
	v_add_f32_e32 v84, v82, v83
	v_lshlrev_b64 v[82:83], 6, v[176:177]
	v_lshl_add_u64 v[82:83], s[10:11], 0, v[82:83]
	v_lshl_add_u64 v[82:83], s[28:29], 2, v[82:83]
	s_lshl_b32 s50, s46, 2
	s_and_b64 vcc, exec, s[4:5]
	v_lshl_add_u64 v[82:83], v[82:83], 0, s[50:51]
	s_cbranch_vccnz .LBB0_860
	global_store_dword v[82:83], v84, off
	s_cbranch_execnz .LBB0_786

; __device__ __forceinline__ void st_wt4(void* p, float v) { asm volatile("global_store_dword %0, %1, off sc1" :: "v"(p), "v"(v) : "memory"); }
; template <int M> __device__ __forceinline__ float xor_add(float v) {
;     if constexpr (M < 32) return v + __int_as_float(__builtin_amdgcn_ds_swizzle(__float_as_int(v), (M << 10) | 0x1f));
;     else { auto rr = __builtin_amdgcn_permlane32_swap(__float_as_uint(v), __float_as_uint(v), false, false); return __uint_as_float(rr[0]) + __uint_as_float(rr[1]); }
;     __device__ __forceinline__ void operator()(const f32x4 (&acc)[2][2][4][2], const Unit& u, int wr, int wc, int fr, int fq) const {
;     ...
;                     ss += ((h0[0] * h0[0] + h0[1] * h0[1]) + (h0[2] * h0[2] + h0[3] * h0[3])) + ((h1[0] * h1[0] + h1[1] * h1[1]) + (h1[2] * h1[2] + h1[3] * h1[3]));
;                 }
;                 ss = xor_add<16>(ss); ss = xor_add<32>(ss);
;                 if (fq == 0) { if (WT && wt) st_wt4(ssqp + SO + (size_t)row * 16 + u.pn * 4 + wc, ss); else ssqp[SO + (size_t)row * 16 + u.pn * 4 + wc] = ss; }
.LBB0_792:
	s_nop 0
	v_mul_f32_e32 v66, v83, v83
	v_mul_f32_e32 v67, v81, v81
	v_fmac_f32_e32 v66, v82, v82
	v_fmac_f32_e32 v67, v80, v80
	v_add_f32_e32 v66, v66, v67
	v_mul_f32_e32 v67, v85, v85
	v_mul_f32_e32 v68, v79, v79
	v_fmac_f32_e32 v67, v84, v84
	v_fmac_f32_e32 v68, v78, v78
	v_add_f32_e32 v67, v67, v68
	v_add_f32_e32 v66, v66, v67
	v_mul_f32_e32 v67, v75, v75
	v_mul_f32_e32 v68, v73, v73
	v_fmac_f32_e32 v67, v74, v74
	v_fmac_f32_e32 v68, v72, v72
	v_add_f32_e32 v67, v67, v68
	v_mul_f32_e32 v68, v77, v77
	v_mul_f32_e32 v69, v71, v71
	v_fmac_f32_e32 v68, v76, v76
	v_fmac_f32_e32 v69, v70, v70
	v_add_f32_e32 v68, v68, v69
	v_add_f32_e32 v67, v67, v68
	v_add_f32_e32 v66, v66, v67
	v_mov_b32_e32 v67, v66
	s_nop 1
	v_permlane16_swap_b32_e32 v66, v67
	s_waitcnt lgkmcnt(0)
	v_add_f32_e32 v66, v66, v67
	v_mov_b32_e32 v67, v66
	s_nop 1
	v_permlane32_swap_b32_e32 v66, v67
	s_and_saveexec_b64 s[30:31], s[6:7]
	s_cbranch_execz .LBB0_796
	v_add_f32_e32 v68, v66, v67
	v_lshlrev_b64 v[66:67], 6, v[172:173]
	v_lshl_add_u64 v[66:67], s[10:11], 0, v[66:67]
	v_lshl_add_u64 v[66:67], s[28:29], 2, v[66:67]
	s_lshl_b32 s50, s46, 2
	s_and_b64 vcc, exec, s[4:5]
	v_lshl_add_u64 v[66:67], v[66:67], 0, s[50:51]
	s_cbranch_vccnz .LBB0_861
	global_store_dword v[66:67], v68, off
	s_cbranch_execnz .LBB0_796

; __device__ __forceinline__ void st_wt4(void* p, float v) { asm volatile("global_store_dword %0, %1, off sc1" :: "v"(p), "v"(v) : "memory"); }
; template <int M> __device__ __forceinline__ float xor_add(float v) {
;     if constexpr (M < 32) return v + __int_as_float(__builtin_amdgcn_ds_swizzle(__float_as_int(v), (M << 10) | 0x1f));
;     else { auto rr = __builtin_amdgcn_permlane32_swap(__float_as_uint(v), __float_as_uint(v), false, false); return __uint_as_float(rr[0]) + __uint_as_float(rr[1]); }
;     __device__ __forceinline__ void operator()(const f32x4 (&acc)[2][2][4][2], const Unit& u, int wr, int wc, int fr, int fq) const {
;     ...
;                     ss += ((h0[0] * h0[0] + h0[1] * h0[1]) + (h0[2] * h0[2] + h0[3] * h0[3])) + ((h1[0] * h1[0] + h1[1] * h1[1]) + (h1[2] * h1[2] + h1[3] * h1[3]));
;                 }
;                 ss = xor_add<16>(ss); ss = xor_add<32>(ss);
;                 if (fq == 0) { if (WT && wt) st_wt4(ssqp + SO + (size_t)row * 16 + u.pn * 4 + wc, ss); else ssqp[SO + (size_t)row * 16 + u.pn * 4 + wc] = ss; }
.LBB0_802:
	s_nop 0
	v_mul_f32_e32 v48, v111, v111
	v_mul_f32_e32 v49, v109, v109
	v_fmac_f32_e32 v48, v110, v110
	v_fmac_f32_e32 v49, v108, v108
	v_add_f32_e32 v48, v48, v49
	v_mul_f32_e32 v49, v63, v63
	v_mul_f32_e32 v50, v61, v61
	v_fmac_f32_e32 v49, v62, v62
	v_fmac_f32_e32 v50, v60, v60
	v_add_f32_e32 v49, v49, v50
	v_add_f32_e32 v48, v48, v49
	v_mul_f32_e32 v49, v57, v57
	v_mul_f32_e32 v50, v55, v55
	v_fmac_f32_e32 v49, v56, v56
	v_fmac_f32_e32 v50, v54, v54
	v_add_f32_e32 v49, v49, v50
	v_mul_f32_e32 v50, v59, v59
	v_mul_f32_e32 v51, v53, v53
	v_fmac_f32_e32 v50, v58, v58
	v_fmac_f32_e32 v51, v52, v52
	v_add_f32_e32 v50, v50, v51
	v_add_f32_e32 v49, v49, v50
	v_add_f32_e32 v48, v48, v49
	v_mov_b32_e32 v49, v48
	s_nop 1
	v_permlane16_swap_b32_e32 v48, v49
	s_waitcnt lgkmcnt(0)
	v_add_f32_e32 v48, v48, v49
	v_mov_b32_e32 v49, v48
	s_nop 1
	v_permlane32_swap_b32_e32 v48, v49
	s_and_saveexec_b64 s[30:31], s[6:7]
	s_cbranch_execz .LBB0_806
	v_add_f32_e32 v50, v48, v49
	v_lshlrev_b64 v[48:49], 6, v[106:107]
	v_lshl_add_u64 v[48:49], s[10:11], 0, v[48:49]
	v_lshl_add_u64 v[48:49], s[28:29], 2, v[48:49]
	s_lshl_b32 s50, s46, 2
	s_and_b64 vcc, exec, s[4:5]
	v_lshl_add_u64 v[48:49], v[48:49], 0, s[50:51]
	s_cbranch_vccnz .LBB0_862
	global_store_dword v[48:49], v50, off
	s_cbranch_execnz .LBB0_806

; __device__ __forceinline__ void st_wt4(void* p, float v) { asm volatile("global_store_dword %0, %1, off sc1" :: "v"(p), "v"(v) : "memory"); }
; template <int M> __device__ __forceinline__ float xor_add(float v) {
;     if constexpr (M < 32) return v + __int_as_float(__builtin_amdgcn_ds_swizzle(__float_as_int(v), (M << 10) | 0x1f));
;     else { auto rr = __builtin_amdgcn_permlane32_swap(__float_as_uint(v), __float_as_uint(v), false, false); return __uint_as_float(rr[0]) + __uint_as_float(rr[1]); }
;     __device__ __forceinline__ void operator()(const f32x4 (&acc)[2][2][4][2], const Unit& u, int wr, int wc, int fr, int fq) const {
;     ...
;                     ss += ((h0[0] * h0[0] + h0[1] * h0[1]) + (h0[2] * h0[2] + h0[3] * h0[3])) + ((h1[0] * h1[0] + h1[1] * h1[1]) + (h1[2] * h1[2] + h1[3] * h1[3]));
;                 }
;                 ss = xor_add<16>(ss); ss = xor_add<32>(ss);
;                 if (fq == 0) { if (WT && wt) st_wt4(ssqp + SO + (size_t)row * 16 + u.pn * 4 + wc, ss); else ssqp[SO + (size_t)row * 16 + u.pn * 4 + wc] = ss; }
.LBB0_812:
	s_nop 0
	v_mul_f32_e32 v32, v49, v49
	v_mul_f32_e32 v33, v39, v39
	v_fmac_f32_e32 v32, v48, v48
	v_fmac_f32_e32 v33, v38, v38
	v_add_f32_e32 v32, v32, v33
	v_mul_f32_e32 v33, v51, v51
	v_mul_f32_e32 v34, v37, v37
	v_fmac_f32_e32 v33, v50, v50
	v_fmac_f32_e32 v34, v36, v36
	v_add_f32_e32 v33, v33, v34
	v_add_f32_e32 v32, v32, v33
	v_mul_f32_e32 v33, v45, v45
	v_mul_f32_e32 v34, v47, v47
	v_fmac_f32_e32 v33, v44, v44
	v_fmac_f32_e32 v34, v46, v46
	v_add_f32_e32 v33, v33, v34
	v_mul_f32_e32 v34, v41, v41
	v_mul_f32_e32 v35, v43, v43
	v_fmac_f32_e32 v34, v40, v40
	v_fmac_f32_e32 v35, v42, v42
	v_add_f32_e32 v34, v34, v35
	v_add_f32_e32 v33, v33, v34
	v_add_f32_e32 v32, v32, v33
	v_mov_b32_e32 v33, v32
	s_nop 1
	v_permlane16_swap_b32_e32 v32, v33
	s_waitcnt lgkmcnt(0)
	v_add_f32_e32 v32, v32, v33
	v_mov_b32_e32 v33, v32
	s_nop 1
	v_permlane32_swap_b32_e32 v32, v33
	s_and_saveexec_b64 s[30:31], s[6:7]
	s_cbranch_execz .LBB0_816
	v_add_f32_e32 v34, v32, v33
	v_lshlrev_b64 v[32:33], 6, v[102:103]
	v_lshl_add_u64 v[32:33], s[10:11], 0, v[32:33]
	v_lshl_add_u64 v[32:33], s[28:29], 2, v[32:33]
	s_lshl_b32 s50, s46, 2
	s_and_b64 vcc, exec, s[4:5]
	v_lshl_add_u64 v[32:33], v[32:33], 0, s[50:51]
	s_cbranch_vccnz .LBB0_863
	global_store_dword v[32:33], v34, off
	s_cbranch_execnz .LBB0_816

; __device__ __forceinline__ void st_wt4(void* p, float v) { asm volatile("global_store_dword %0, %1, off sc1" :: "v"(p), "v"(v) : "memory"); }
; template <int M> __device__ __forceinline__ float xor_add(float v) {
;     if constexpr (M < 32) return v + __int_as_float(__builtin_amdgcn_ds_swizzle(__float_as_int(v), (M << 10) | 0x1f));
;     else { auto rr = __builtin_amdgcn_permlane32_swap(__float_as_uint(v), __float_as_uint(v), false, false); return __uint_as_float(rr[0]) + __uint_as_float(rr[1]); }
;     __device__ __forceinline__ void operator()(const f32x4 (&acc)[2][2][4][2], const Unit& u, int wr, int wc, int fr, int fq) const {
;     ...
;                     ss += ((h0[0] * h0[0] + h0[1] * h0[1]) + (h0[2] * h0[2] + h0[3] * h0[3])) + ((h1[0] * h1[0] + h1[1] * h1[1]) + (h1[2] * h1[2] + h1[3] * h1[3]));
;                 }
;                 ss = xor_add<16>(ss); ss = xor_add<32>(ss);
;                 if (fq == 0) { if (WT && wt) st_wt4(ssqp + SO + (size_t)row * 16 + u.pn * 4 + wc, ss); else ssqp[SO + (size_t)row * 16 + u.pn * 4 + wc] = ss; }
.LBB0_822:
	s_nop 0
	v_mul_f32_e32 v16, v33, v33
	v_mul_f32_e32 v17, v23, v23
	v_fmac_f32_e32 v16, v32, v32
	v_fmac_f32_e32 v17, v22, v22
	v_add_f32_e32 v16, v16, v17
	v_mul_f32_e32 v17, v35, v35
	v_mul_f32_e32 v18, v21, v21
	v_fmac_f32_e32 v17, v34, v34
	v_fmac_f32_e32 v18, v20, v20
	v_add_f32_e32 v17, v17, v18
	v_add_f32_e32 v16, v16, v17
	v_mul_f32_e32 v17, v29, v29
	v_mul_f32_e32 v18, v31, v31
	v_fmac_f32_e32 v17, v28, v28
	v_fmac_f32_e32 v18, v30, v30
	v_add_f32_e32 v17, v17, v18
	v_mul_f32_e32 v18, v25, v25
	v_mul_f32_e32 v19, v27, v27
	v_fmac_f32_e32 v18, v24, v24
	v_fmac_f32_e32 v19, v26, v26
	v_add_f32_e32 v18, v18, v19
	v_add_f32_e32 v17, v17, v18
	v_add_f32_e32 v16, v16, v17
	v_mov_b32_e32 v17, v16
	s_nop 1
	v_permlane16_swap_b32_e32 v16, v17
	s_waitcnt lgkmcnt(0)
	v_add_f32_e32 v16, v16, v17
	v_mov_b32_e32 v17, v16
	s_nop 1
	v_permlane32_swap_b32_e32 v16, v17
	s_and_saveexec_b64 s[30:31], s[6:7]
	s_cbranch_execz .LBB0_826
	v_add_f32_e32 v18, v16, v17
	v_lshlrev_b64 v[16:17], 6, v[98:99]
	v_lshl_add_u64 v[16:17], s[10:11], 0, v[16:17]
	v_lshl_add_u64 v[16:17], s[28:29], 2, v[16:17]
	s_lshl_b32 s50, s46, 2
	s_and_b64 vcc, exec, s[4:5]
	v_lshl_add_u64 v[16:17], v[16:17], 0, s[50:51]
	s_cbranch_vccnz .LBB0_864
	global_store_dword v[16:17], v18, off
	s_cbranch_execnz .LBB0_826

; __device__ __forceinline__ void st_wt4(void* p, float v) { asm volatile("global_store_dword %0, %1, off sc1" :: "v"(p), "v"(v) : "memory"); }
; template <int M> __device__ __forceinline__ float xor_add(float v) {
;     if constexpr (M < 32) return v + __int_as_float(__builtin_amdgcn_ds_swizzle(__float_as_int(v), (M << 10) | 0x1f));
;     else { auto rr = __builtin_amdgcn_permlane32_swap(__float_as_uint(v), __float_as_uint(v), false, false); return __uint_as_float(rr[0]) + __uint_as_float(rr[1]); }
;     __device__ __forceinline__ void operator()(const f32x4 (&acc)[2][2][4][2], const Unit& u, int wr, int wc, int fr, int fq) const {
;     ...
;                     ss += ((h0[0] * h0[0] + h0[1] * h0[1]) + (h0[2] * h0[2] + h0[3] * h0[3])) + ((h1[0] * h1[0] + h1[1] * h1[1]) + (h1[2] * h1[2] + h1[3] * h1[3]));
;                 }
;                 ss = xor_add<16>(ss); ss = xor_add<32>(ss);
;                 if (fq == 0) { if (WT && wt) st_wt4(ssqp + SO + (size_t)row * 16 + u.pn * 4 + wc, ss); else ssqp[SO + (size_t)row * 16 + u.pn * 4 + wc] = ss; }
.LBB0_832:
	s_nop 0
	v_mul_f32_e32 v0, v17, v17
	v_mul_f32_e32 v1, v7, v7
	v_fmac_f32_e32 v0, v16, v16
	v_fmac_f32_e32 v1, v6, v6
	v_add_f32_e32 v0, v0, v1
	v_mul_f32_e32 v1, v19, v19
	v_mul_f32_e32 v2, v5, v5
	v_fmac_f32_e32 v1, v18, v18
	v_fmac_f32_e32 v2, v4, v4
	v_add_f32_e32 v1, v1, v2
	v_add_f32_e32 v0, v0, v1
	v_mul_f32_e32 v1, v13, v13
	v_mul_f32_e32 v2, v15, v15
	v_fmac_f32_e32 v1, v12, v12
	v_fmac_f32_e32 v2, v14, v14
	v_add_f32_e32 v1, v1, v2
	v_mul_f32_e32 v2, v9, v9
	v_mul_f32_e32 v3, v11, v11
	v_fmac_f32_e32 v2, v8, v8
	v_fmac_f32_e32 v3, v10, v10
	v_add_f32_e32 v2, v2, v3
	v_add_f32_e32 v1, v1, v2
	v_add_f32_e32 v0, v0, v1
	v_mov_b32_e32 v1, v0
	s_nop 1
	v_permlane16_swap_b32_e32 v0, v1
	s_waitcnt lgkmcnt(0)
	v_add_f32_e32 v0, v0, v1
	v_mov_b32_e32 v1, v0
	s_nop 1
	v_permlane32_swap_b32_e32 v0, v1
	s_and_saveexec_b64 s[30:31], s[6:7]
	s_cbranch_execz .LBB0_836
	v_add_f32_e32 v2, v0, v1
	v_lshlrev_b64 v[0:1], 6, v[94:95]
	v_lshl_add_u64 v[0:1], s[10:11], 0, v[0:1]
	v_lshl_add_u64 v[0:1], s[28:29], 2, v[0:1]
	s_lshl_b32 s50, s46, 2
	s_and_b64 vcc, exec, s[4:5]
	v_lshl_add_u64 v[0:1], v[0:1], 0, s[50:51]
	s_cbranch_vccnz .LBB0_865
	global_store_dword v[0:1], v2, off
	s_cbranch_execnz .LBB0_836

; __device__ __forceinline__ void st_wt4(void* p, float v) { asm volatile("global_store_dword %0, %1, off sc1" :: "v"(p), "v"(v) : "memory"); }
; template <int M> __device__ __forceinline__ float xor_add(float v) {
;     if constexpr (M < 32) return v + __int_as_float(__builtin_amdgcn_ds_swizzle(__float_as_int(v), (M << 10) | 0x1f));
;     else { auto rr = __builtin_amdgcn_permlane32_swap(__float_as_uint(v), __float_as_uint(v), false, false); return __uint_as_float(rr[0]) + __uint_as_float(rr[1]); }
;     __device__ __forceinline__ void operator()(const f32x4 (&acc)[2][2][4][2], const Unit& u, int wr, int wc, int fr, int fq) const {
;     ...
;                     ss += ((h0[0] * h0[0] + h0[1] * h0[1]) + (h0[2] * h0[2] + h0[3] * h0[3])) + ((h1[0] * h1[0] + h1[1] * h1[1]) + (h1[2] * h1[2] + h1[3] * h1[3]));
;                 }
;                 ss = xor_add<16>(ss); ss = xor_add<32>(ss);
;                 if (fq == 0) { if (WT && wt) st_wt4(ssqp + SO + (size_t)row * 16 + u.pn * 4 + wc, ss); else ssqp[SO + (size_t)row * 16 + u.pn * 4 + wc] = ss; }
.LBB0_897:
	s_nop 0
	v_mul_f32_e32 v114, v211, v211
	v_mul_f32_e32 v115, v209, v209
	v_fmac_f32_e32 v114, v210, v210
	v_fmac_f32_e32 v115, v208, v208
	v_add_f32_e32 v114, v114, v115
	v_mul_f32_e32 v115, v129, v129
	v_mul_f32_e32 v116, v127, v127
	v_fmac_f32_e32 v115, v128, v128
	v_fmac_f32_e32 v116, v126, v126
	v_add_f32_e32 v115, v115, v116
	v_add_f32_e32 v114, v114, v115
	v_mul_f32_e32 v115, v123, v123
	v_mul_f32_e32 v116, v121, v121
	v_fmac_f32_e32 v115, v122, v122
	v_fmac_f32_e32 v116, v120, v120
	v_add_f32_e32 v115, v115, v116
	v_mul_f32_e32 v116, v125, v125
	v_mul_f32_e32 v117, v119, v119
	v_fmac_f32_e32 v116, v124, v124
	v_fmac_f32_e32 v117, v118, v118
	v_add_f32_e32 v116, v116, v117
	v_add_f32_e32 v115, v115, v116
	v_add_f32_e32 v114, v114, v115
	v_mov_b32_e32 v115, v114
	s_nop 1
	v_permlane16_swap_b32_e32 v114, v115
	s_lshl_b32 s28, s28, 2
	v_cmp_eq_u32_e64 s[6:7], 0, v217
	s_ashr_i32 s29, s28, 31
	s_waitcnt lgkmcnt(0)
	v_add_f32_e32 v114, v114, v115
	v_mov_b32_e32 v115, v114
	s_nop 1
	v_permlane32_swap_b32_e32 v114, v115
	s_and_saveexec_b64 s[30:31], s[6:7]
	s_cbranch_execz .LBB0_901
	v_add_f32_e32 v116, v114, v115
	v_lshlrev_b64 v[114:115], 6, v[198:199]
	v_lshl_add_u64 v[114:115], s[10:11], 0, v[114:115]
	v_lshl_add_u64 v[114:115], s[28:29], 2, v[114:115]
	s_lshl_b32 s50, s46, 2
	v_lshl_add_u64 v[114:115], v[114:115], 0, s[50:51]
	s_and_b64 vcc, exec, s[12:13]
	s_cbranch_vccz .LBB0_993
	global_store_dword v[114:115], v116, off
	s_cbranch_execnz .LBB0_901

; __device__ __forceinline__ void st_wt4(void* p, float v) { asm volatile("global_store_dword %0, %1, off sc1" :: "v"(p), "v"(v) : "memory"); }
; template <int M> __device__ __forceinline__ float xor_add(float v) {
;     if constexpr (M < 32) return v + __int_as_float(__builtin_amdgcn_ds_swizzle(__float_as_int(v), (M << 10) | 0x1f));
;     else { auto rr = __builtin_amdgcn_permlane32_swap(__float_as_uint(v), __float_as_uint(v), false, false); return __uint_as_float(rr[0]) + __uint_as_float(rr[1]); }
;     __device__ __forceinline__ void operator()(const f32x4 (&acc)[2][2][4][2], const Unit& u, int wr, int wc, int fr, int fq) const {
;     ...
;                     ss += ((h0[0] * h0[0] + h0[1] * h0[1]) + (h0[2] * h0[2] + h0[3] * h0[3])) + ((h1[0] * h1[0] + h1[1] * h1[1]) + (h1[2] * h1[2] + h1[3] * h1[3]));
;                 }
;                 ss = xor_add<16>(ss); ss = xor_add<32>(ss);
;                 if (fq == 0) { if (WT && wt) st_wt4(ssqp + SO + (size_t)row * 16 + u.pn * 4 + wc, ss); else ssqp[SO + (size_t)row * 16 + u.pn * 4 + wc] = ss; }
.LBB0_907:
	s_nop 0
	v_mul_f32_e32 v98, v115, v115
	v_mul_f32_e32 v99, v113, v113
	v_fmac_f32_e32 v98, v114, v114
	v_fmac_f32_e32 v99, v112, v112
	v_add_f32_e32 v98, v98, v99
	v_mul_f32_e32 v99, v117, v117
	v_mul_f32_e32 v100, v111, v111
	v_fmac_f32_e32 v99, v116, v116
	v_fmac_f32_e32 v100, v110, v110
	v_add_f32_e32 v99, v99, v100
	v_add_f32_e32 v98, v98, v99
	v_mul_f32_e32 v99, v107, v107
	v_mul_f32_e32 v100, v105, v105
	v_fmac_f32_e32 v99, v106, v106
	v_fmac_f32_e32 v100, v104, v104
	v_add_f32_e32 v99, v99, v100
	v_mul_f32_e32 v100, v109, v109
	v_mul_f32_e32 v101, v103, v103
	v_fmac_f32_e32 v100, v108, v108
	v_fmac_f32_e32 v101, v102, v102
	v_add_f32_e32 v100, v100, v101
	v_add_f32_e32 v99, v99, v100
	v_add_f32_e32 v98, v98, v99
	v_mov_b32_e32 v99, v98
	s_nop 1
	v_permlane16_swap_b32_e32 v98, v99
	s_waitcnt lgkmcnt(0)
	v_add_f32_e32 v98, v98, v99
	v_mov_b32_e32 v99, v98
	s_nop 1
	v_permlane32_swap_b32_e32 v98, v99
	s_and_saveexec_b64 s[30:31], s[6:7]
	s_cbranch_execz .LBB0_911
	v_add_f32_e32 v100, v98, v99
	v_lshlrev_b64 v[98:99], 6, v[206:207]
	v_lshl_add_u64 v[98:99], s[10:11], 0, v[98:99]
	v_lshl_add_u64 v[98:99], s[28:29], 2, v[98:99]
	s_lshl_b32 s50, s46, 2
	s_and_b64 vcc, exec, s[4:5]
	v_lshl_add_u64 v[98:99], v[98:99], 0, s[50:51]
	s_cbranch_vccnz .LBB0_994
	global_store_dword v[98:99], v100, off
	s_cbranch_execnz .LBB0_911

; __device__ __forceinline__ void st_wt4(void* p, float v) { asm volatile("global_store_dword %0, %1, off sc1" :: "v"(p), "v"(v) : "memory"); }
; template <int M> __device__ __forceinline__ float xor_add(float v) {
;     if constexpr (M < 32) return v + __int_as_float(__builtin_amdgcn_ds_swizzle(__float_as_int(v), (M << 10) | 0x1f));
;     else { auto rr = __builtin_amdgcn_permlane32_swap(__float_as_uint(v), __float_as_uint(v), false, false); return __uint_as_float(rr[0]) + __uint_as_float(rr[1]); }
;     __device__ __forceinline__ void operator()(const f32x4 (&acc)[2][2][4][2], const Unit& u, int wr, int wc, int fr, int fq) const {
;     ...
;                     ss += ((h0[0] * h0[0] + h0[1] * h0[1]) + (h0[2] * h0[2] + h0[3] * h0[3])) + ((h1[0] * h1[0] + h1[1] * h1[1]) + (h1[2] * h1[2] + h1[3] * h1[3]));
;                 }
;                 ss = xor_add<16>(ss); ss = xor_add<32>(ss);
;                 if (fq == 0) { if (WT && wt) st_wt4(ssqp + SO + (size_t)row * 16 + u.pn * 4 + wc, ss); else ssqp[SO + (size_t)row * 16 + u.pn * 4 + wc] = ss; }
.LBB0_917:
	s_nop 0
	v_mul_f32_e32 v82, v99, v99
	v_mul_f32_e32 v83, v97, v97
	v_fmac_f32_e32 v82, v98, v98
	v_fmac_f32_e32 v83, v96, v96
	v_add_f32_e32 v82, v82, v83
	v_mul_f32_e32 v83, v101, v101
	v_mul_f32_e32 v84, v95, v95
	v_fmac_f32_e32 v83, v100, v100
	v_fmac_f32_e32 v84, v94, v94
	v_add_f32_e32 v83, v83, v84
	v_add_f32_e32 v82, v82, v83
	v_mul_f32_e32 v83, v91, v91
	v_mul_f32_e32 v84, v89, v89
	v_fmac_f32_e32 v83, v90, v90
	v_fmac_f32_e32 v84, v88, v88
	v_add_f32_e32 v83, v83, v84
	v_mul_f32_e32 v84, v93, v93
	v_mul_f32_e32 v85, v87, v87
	v_fmac_f32_e32 v84, v92, v92
	v_fmac_f32_e32 v85, v86, v86
	v_add_f32_e32 v84, v84, v85
	v_add_f32_e32 v83, v83, v84
	v_add_f32_e32 v82, v82, v83
	v_mov_b32_e32 v83, v82
	s_nop 1
	v_permlane16_swap_b32_e32 v82, v83
	s_waitcnt lgkmcnt(0)
	v_add_f32_e32 v82, v82, v83
	v_mov_b32_e32 v83, v82
	s_nop 1
	v_permlane32_swap_b32_e32 v82, v83
	s_and_saveexec_b64 s[30:31], s[6:7]
	s_cbranch_execz .LBB0_921
	v_add_f32_e32 v84, v82, v83
	v_lshlrev_b64 v[82:83], 6, v[204:205]
	v_lshl_add_u64 v[82:83], s[10:11], 0, v[82:83]
	v_lshl_add_u64 v[82:83], s[28:29], 2, v[82:83]
	s_lshl_b32 s50, s46, 2
	s_and_b64 vcc, exec, s[4:5]
	v_lshl_add_u64 v[82:83], v[82:83], 0, s[50:51]
	s_cbranch_vccnz .LBB0_995
	global_store_dword v[82:83], v84, off
	s_cbranch_execnz .LBB0_921

; __device__ __forceinline__ void st_wt4(void* p, float v) { asm volatile("global_store_dword %0, %1, off sc1" :: "v"(p), "v"(v) : "memory"); }
; template <int M> __device__ __forceinline__ float xor_add(float v) {
;     if constexpr (M < 32) return v + __int_as_float(__builtin_amdgcn_ds_swizzle(__float_as_int(v), (M << 10) | 0x1f));
;     else { auto rr = __builtin_amdgcn_permlane32_swap(__float_as_uint(v), __float_as_uint(v), false, false); return __uint_as_float(rr[0]) + __uint_as_float(rr[1]); }
;     __device__ __forceinline__ void operator()(const f32x4 (&acc)[2][2][4][2], const Unit& u, int wr, int wc, int fr, int fq) const {
;     ...
;                     ss += ((h0[0] * h0[0] + h0[1] * h0[1]) + (h0[2] * h0[2] + h0[3] * h0[3])) + ((h1[0] * h1[0] + h1[1] * h1[1]) + (h1[2] * h1[2] + h1[3] * h1[3]));
;                 }
;                 ss = xor_add<16>(ss); ss = xor_add<32>(ss);
;                 if (fq == 0) { if (WT && wt) st_wt4(ssqp + SO + (size_t)row * 16 + u.pn * 4 + wc, ss); else ssqp[SO + (size_t)row * 16 + u.pn * 4 + wc] = ss; }
.LBB0_927:
	s_nop 0
	v_mul_f32_e32 v66, v83, v83
	v_mul_f32_e32 v67, v81, v81
	v_fmac_f32_e32 v66, v82, v82
	v_fmac_f32_e32 v67, v80, v80
	v_add_f32_e32 v66, v66, v67
	v_mul_f32_e32 v67, v85, v85
	v_mul_f32_e32 v68, v79, v79
	v_fmac_f32_e32 v67, v84, v84
	v_fmac_f32_e32 v68, v78, v78
	v_add_f32_e32 v67, v67, v68
	v_add_f32_e32 v66, v66, v67
	v_mul_f32_e32 v67, v75, v75
	v_mul_f32_e32 v68, v73, v73
	v_fmac_f32_e32 v67, v74, v74
	v_fmac_f32_e32 v68, v72, v72
	v_add_f32_e32 v67, v67, v68
	v_mul_f32_e32 v68, v77, v77
	v_mul_f32_e32 v69, v71, v71
	v_fmac_f32_e32 v68, v76, v76
	v_fmac_f32_e32 v69, v70, v70
	v_add_f32_e32 v68, v68, v69
	v_add_f32_e32 v67, v67, v68
	v_add_f32_e32 v66, v66, v67
	v_mov_b32_e32 v67, v66
	s_nop 1
	v_permlane16_swap_b32_e32 v66, v67
	s_waitcnt lgkmcnt(0)
	v_add_f32_e32 v66, v66, v67
	v_mov_b32_e32 v67, v66
	s_nop 1
	v_permlane32_swap_b32_e32 v66, v67
	s_and_saveexec_b64 s[30:31], s[6:7]
	s_cbranch_execz .LBB0_931
	v_add_f32_e32 v68, v66, v67
	v_lshlrev_b64 v[66:67], 6, v[202:203]
	v_lshl_add_u64 v[66:67], s[10:11], 0, v[66:67]
	v_lshl_add_u64 v[66:67], s[28:29], 2, v[66:67]
	s_lshl_b32 s50, s46, 2
	s_and_b64 vcc, exec, s[4:5]
	v_lshl_add_u64 v[66:67], v[66:67], 0, s[50:51]
	s_cbranch_vccnz .LBB0_996
	global_store_dword v[66:67], v68, off
	s_cbranch_execnz .LBB0_931

; __device__ __forceinline__ void st_wt4(void* p, float v) { asm volatile("global_store_dword %0, %1, off sc1" :: "v"(p), "v"(v) : "memory"); }
; template <int M> __device__ __forceinline__ float xor_add(float v) {
;     if constexpr (M < 32) return v + __int_as_float(__builtin_amdgcn_ds_swizzle(__float_as_int(v), (M << 10) | 0x1f));
;     else { auto rr = __builtin_amdgcn_permlane32_swap(__float_as_uint(v), __float_as_uint(v), false, false); return __uint_as_float(rr[0]) + __uint_as_float(rr[1]); }
;     __device__ __forceinline__ void operator()(const f32x4 (&acc)[2][2][4][2], const Unit& u, int wr, int wc, int fr, int fq) const {
;     ...
;                     ss += ((h0[0] * h0[0] + h0[1] * h0[1]) + (h0[2] * h0[2] + h0[3] * h0[3])) + ((h1[0] * h1[0] + h1[1] * h1[1]) + (h1[2] * h1[2] + h1[3] * h1[3]));
;                 }
;                 ss = xor_add<16>(ss); ss = xor_add<32>(ss);
;                 if (fq == 0) { if (WT && wt) st_wt4(ssqp + SO + (size_t)row * 16 + u.pn * 4 + wc, ss); else ssqp[SO + (size_t)row * 16 + u.pn * 4 + wc] = ss; }
.LBB0_937:
	s_nop 0
	v_mul_f32_e32 v48, v133, v133
	v_mul_f32_e32 v49, v131, v131
	v_fmac_f32_e32 v48, v132, v132
	v_fmac_f32_e32 v49, v130, v130
	v_add_f32_e32 v48, v48, v49
	v_mul_f32_e32 v49, v63, v63
	v_mul_f32_e32 v50, v61, v61
	v_fmac_f32_e32 v49, v62, v62
	v_fmac_f32_e32 v50, v60, v60
	v_add_f32_e32 v49, v49, v50
	v_add_f32_e32 v48, v48, v49
	v_mul_f32_e32 v49, v57, v57
	v_mul_f32_e32 v50, v55, v55
	v_fmac_f32_e32 v49, v56, v56
	v_fmac_f32_e32 v50, v54, v54
	v_add_f32_e32 v49, v49, v50
	v_mul_f32_e32 v50, v59, v59
	v_mul_f32_e32 v51, v53, v53
	v_fmac_f32_e32 v50, v58, v58
	v_fmac_f32_e32 v51, v52, v52
	v_add_f32_e32 v50, v50, v51
	v_add_f32_e32 v49, v49, v50
	v_add_f32_e32 v48, v48, v49
	v_mov_b32_e32 v49, v48
	s_nop 1
	v_permlane16_swap_b32_e32 v48, v49
	s_waitcnt lgkmcnt(0)
	v_add_f32_e32 v48, v48, v49
	v_mov_b32_e32 v49, v48
	s_nop 1
	v_permlane32_swap_b32_e32 v48, v49
	s_and_saveexec_b64 s[30:31], s[6:7]
	s_cbranch_execz .LBB0_941
	v_add_f32_e32 v50, v48, v49
	v_lshlrev_b64 v[48:49], 6, v[128:129]
	v_lshl_add_u64 v[48:49], s[10:11], 0, v[48:49]
	v_lshl_add_u64 v[48:49], s[28:29], 2, v[48:49]
	s_lshl_b32 s50, s46, 2
	s_and_b64 vcc, exec, s[4:5]
	v_lshl_add_u64 v[48:49], v[48:49], 0, s[50:51]
	s_cbranch_vccnz .LBB0_997
	global_store_dword v[48:49], v50, off
	s_cbranch_execnz .LBB0_941

; __device__ __forceinline__ void st_wt4(void* p, float v) { asm volatile("global_store_dword %0, %1, off sc1" :: "v"(p), "v"(v) : "memory"); }
; template <int M> __device__ __forceinline__ float xor_add(float v) {
;     if constexpr (M < 32) return v + __int_as_float(__builtin_amdgcn_ds_swizzle(__float_as_int(v), (M << 10) | 0x1f));
;     else { auto rr = __builtin_amdgcn_permlane32_swap(__float_as_uint(v), __float_as_uint(v), false, false); return __uint_as_float(rr[0]) + __uint_as_float(rr[1]); }
;     __device__ __forceinline__ void operator()(const f32x4 (&acc)[2][2][4][2], const Unit& u, int wr, int wc, int fr, int fq) const {
;     ...
;                     ss += ((h0[0] * h0[0] + h0[1] * h0[1]) + (h0[2] * h0[2] + h0[3] * h0[3])) + ((h1[0] * h1[0] + h1[1] * h1[1]) + (h1[2] * h1[2] + h1[3] * h1[3]));
;                 }
;                 ss = xor_add<16>(ss); ss = xor_add<32>(ss);
;                 if (fq == 0) { if (WT && wt) st_wt4(ssqp + SO + (size_t)row * 16 + u.pn * 4 + wc, ss); else ssqp[SO + (size_t)row * 16 + u.pn * 4 + wc] = ss; }
.LBB0_947:
	s_nop 0
	v_mul_f32_e32 v32, v49, v49
	v_mul_f32_e32 v33, v39, v39
	v_fmac_f32_e32 v32, v48, v48
	v_fmac_f32_e32 v33, v38, v38
	v_add_f32_e32 v32, v32, v33
	v_mul_f32_e32 v33, v51, v51
	v_mul_f32_e32 v34, v37, v37
	v_fmac_f32_e32 v33, v50, v50
	v_fmac_f32_e32 v34, v36, v36
	v_add_f32_e32 v33, v33, v34
	v_add_f32_e32 v32, v32, v33
	v_mul_f32_e32 v33, v45, v45
	v_mul_f32_e32 v34, v47, v47
	v_fmac_f32_e32 v33, v44, v44
	v_fmac_f32_e32 v34, v46, v46
	v_add_f32_e32 v33, v33, v34
	v_mul_f32_e32 v34, v41, v41
	v_mul_f32_e32 v35, v43, v43
	v_fmac_f32_e32 v34, v40, v40
	v_fmac_f32_e32 v35, v42, v42
	v_add_f32_e32 v34, v34, v35
	v_add_f32_e32 v33, v33, v34
	v_add_f32_e32 v32, v32, v33
	v_mov_b32_e32 v33, v32
	s_nop 1
	v_permlane16_swap_b32_e32 v32, v33
	s_waitcnt lgkmcnt(0)
	v_add_f32_e32 v32, v32, v33
	v_mov_b32_e32 v33, v32
	s_nop 1
	v_permlane32_swap_b32_e32 v32, v33
	s_and_saveexec_b64 s[30:31], s[6:7]
	s_cbranch_execz .LBB0_951
	v_add_f32_e32 v34, v32, v33
	v_lshlrev_b64 v[32:33], 6, v[126:127]
	v_lshl_add_u64 v[32:33], s[10:11], 0, v[32:33]
	v_lshl_add_u64 v[32:33], s[28:29], 2, v[32:33]
	s_lshl_b32 s50, s46, 2
	s_and_b64 vcc, exec, s[4:5]
	v_lshl_add_u64 v[32:33], v[32:33], 0, s[50:51]
	s_cbranch_vccnz .LBB0_998
	global_store_dword v[32:33], v34, off
	s_cbranch_execnz .LBB0_951

; __device__ __forceinline__ void st_wt4(void* p, float v) { asm volatile("global_store_dword %0, %1, off sc1" :: "v"(p), "v"(v) : "memory"); }
; template <int M> __device__ __forceinline__ float xor_add(float v) {
;     if constexpr (M < 32) return v + __int_as_float(__builtin_amdgcn_ds_swizzle(__float_as_int(v), (M << 10) | 0x1f));
;     else { auto rr = __builtin_amdgcn_permlane32_swap(__float_as_uint(v), __float_as_uint(v), false, false); return __uint_as_float(rr[0]) + __uint_as_float(rr[1]); }
;     __device__ __forceinline__ void operator()(const f32x4 (&acc)[2][2][4][2], const Unit& u, int wr, int wc, int fr, int fq) const {
;     ...
;                     ss += ((h0[0] * h0[0] + h0[1] * h0[1]) + (h0[2] * h0[2] + h0[3] * h0[3])) + ((h1[0] * h1[0] + h1[1] * h1[1]) + (h1[2] * h1[2] + h1[3] * h1[3]));
;                 }
;                 ss = xor_add<16>(ss); ss = xor_add<32>(ss);
;                 if (fq == 0) { if (WT && wt) st_wt4(ssqp + SO + (size_t)row * 16 + u.pn * 4 + wc, ss); else ssqp[SO + (size_t)row * 16 + u.pn * 4 + wc] = ss; }
.LBB0_957:
	s_nop 0
	v_mul_f32_e32 v16, v33, v33
	v_mul_f32_e32 v17, v23, v23
	v_fmac_f32_e32 v16, v32, v32
	v_fmac_f32_e32 v17, v22, v22
	v_add_f32_e32 v16, v16, v17
	v_mul_f32_e32 v17, v35, v35
	v_mul_f32_e32 v18, v21, v21
	v_fmac_f32_e32 v17, v34, v34
	v_fmac_f32_e32 v18, v20, v20
	v_add_f32_e32 v17, v17, v18
	v_add_f32_e32 v16, v16, v17
	v_mul_f32_e32 v17, v29, v29
	v_mul_f32_e32 v18, v31, v31
	v_fmac_f32_e32 v17, v28, v28
	v_fmac_f32_e32 v18, v30, v30
	v_add_f32_e32 v17, v17, v18
	v_mul_f32_e32 v18, v25, v25
	v_mul_f32_e32 v19, v27, v27
	v_fmac_f32_e32 v18, v24, v24
	v_fmac_f32_e32 v19, v26, v26
	v_add_f32_e32 v18, v18, v19
	v_add_f32_e32 v17, v17, v18
	v_add_f32_e32 v16, v16, v17
	v_mov_b32_e32 v17, v16
	s_nop 1
	v_permlane16_swap_b32_e32 v16, v17
	s_waitcnt lgkmcnt(0)
	v_add_f32_e32 v16, v16, v17
	v_mov_b32_e32 v17, v16
	s_nop 1
	v_permlane32_swap_b32_e32 v16, v17
	s_and_saveexec_b64 s[30:31], s[6:7]
	s_cbranch_execz .LBB0_961
	v_add_f32_e32 v18, v16, v17
	v_lshlrev_b64 v[16:17], 6, v[124:125]
	v_lshl_add_u64 v[16:17], s[10:11], 0, v[16:17]
	v_lshl_add_u64 v[16:17], s[28:29], 2, v[16:17]
	s_lshl_b32 s50, s46, 2
	s_and_b64 vcc, exec, s[4:5]
	v_lshl_add_u64 v[16:17], v[16:17], 0, s[50:51]
	s_cbranch_vccnz .LBB0_999
	global_store_dword v[16:17], v18, off
	s_cbranch_execnz .LBB0_961

; __device__ __forceinline__ void st_wt4(void* p, float v) { asm volatile("global_store_dword %0, %1, off sc1" :: "v"(p), "v"(v) : "memory"); }
; template <int M> __device__ __forceinline__ float xor_add(float v) {
;     if constexpr (M < 32) return v + __int_as_float(__builtin_amdgcn_ds_swizzle(__float_as_int(v), (M << 10) | 0x1f));
;     else { auto rr = __builtin_amdgcn_permlane32_swap(__float_as_uint(v), __float_as_uint(v), false, false); return __uint_as_float(rr[0]) + __uint_as_float(rr[1]); }
;     __device__ __forceinline__ void operator()(const f32x4 (&acc)[2][2][4][2], const Unit& u, int wr, int wc, int fr, int fq) const {
;     ...
;                     ss += ((h0[0] * h0[0] + h0[1] * h0[1]) + (h0[2] * h0[2] + h0[3] * h0[3])) + ((h1[0] * h1[0] + h1[1] * h1[1]) + (h1[2] * h1[2] + h1[3] * h1[3]));
;                 }
;                 ss = xor_add<16>(ss); ss = xor_add<32>(ss);
;                 if (fq == 0) { if (WT && wt) st_wt4(ssqp + SO + (size_t)row * 16 + u.pn * 4 + wc, ss); else ssqp[SO + (size_t)row * 16 + u.pn * 4 + wc] = ss; }
.LBB0_967:
	s_nop 0
	v_mul_f32_e32 v0, v17, v17
	v_mul_f32_e32 v1, v7, v7
	v_fmac_f32_e32 v0, v16, v16
	v_fmac_f32_e32 v1, v6, v6
	v_add_f32_e32 v0, v0, v1
	v_mul_f32_e32 v1, v19, v19
	v_mul_f32_e32 v2, v5, v5
	v_fmac_f32_e32 v1, v18, v18
	v_fmac_f32_e32 v2, v4, v4
	v_add_f32_e32 v1, v1, v2
	v_add_f32_e32 v0, v0, v1
	v_mul_f32_e32 v1, v13, v13
	v_mul_f32_e32 v2, v15, v15
	v_fmac_f32_e32 v1, v12, v12
	v_fmac_f32_e32 v2, v14, v14
	v_add_f32_e32 v1, v1, v2
	v_mul_f32_e32 v2, v9, v9
	v_mul_f32_e32 v3, v11, v11
	v_fmac_f32_e32 v2, v8, v8
	v_fmac_f32_e32 v3, v10, v10
	v_add_f32_e32 v2, v2, v3
	v_add_f32_e32 v1, v1, v2
	v_add_f32_e32 v0, v0, v1
	v_mov_b32_e32 v1, v0
	s_nop 1
	v_permlane16_swap_b32_e32 v0, v1
	s_waitcnt lgkmcnt(0)
	v_add_f32_e32 v0, v0, v1
	v_mov_b32_e32 v1, v0
	s_nop 1
	v_permlane32_swap_b32_e32 v0, v1
	s_and_saveexec_b64 s[30:31], s[6:7]
	s_cbranch_execz .LBB0_971
	v_add_f32_e32 v2, v0, v1
	v_lshlrev_b64 v[0:1], 6, v[122:123]
	v_lshl_add_u64 v[0:1], s[10:11], 0, v[0:1]
	v_lshl_add_u64 v[0:1], s[28:29], 2, v[0:1]
	s_lshl_b32 s50, s46, 2
	s_and_b64 vcc, exec, s[4:5]
	v_lshl_add_u64 v[0:1], v[0:1], 0, s[50:51]
	s_cbranch_vccnz .LBB0_1000
	global_store_dword v[0:1], v2, off
	s_cbranch_execnz .LBB0_971

; __device__ __forceinline__ void st_wt4(void* p, float v) { asm volatile("global_store_dword %0, %1, off sc1" :: "v"(p), "v"(v) : "memory"); }
; template <int M> __device__ __forceinline__ float xor_add(float v) {
;     if constexpr (M < 32) return v + __int_as_float(__builtin_amdgcn_ds_swizzle(__float_as_int(v), (M << 10) | 0x1f));
;     else { auto rr = __builtin_amdgcn_permlane32_swap(__float_as_uint(v), __float_as_uint(v), false, false); return __uint_as_float(rr[0]) + __uint_as_float(rr[1]); }
;     __device__ __forceinline__ void operator()(const f32x4 (&acc)[2][2][4][2], const Unit& u, int wr, int wc, int fr, int fq) const {
;     ...
;                     ss += ((h0[0] * h0[0] + h0[1] * h0[1]) + (h0[2] * h0[2] + h0[3] * h0[3])) + ((h1[0] * h1[0] + h1[1] * h1[1]) + (h1[2] * h1[2] + h1[3] * h1[3]));
;                 }
;                 ss = xor_add<16>(ss); ss = xor_add<32>(ss);
;                 if (fq == 0) { if (WT && wt) st_wt4(ssqp + SO + (size_t)row * 16 + u.pn * 4 + wc, ss); else ssqp[SO + (size_t)row * 16 + u.pn * 4 + wc] = ss; }
.LBB0_1311:
	s_nop 0
	v_mul_f32_e32 v114, v183, v183
	v_mul_f32_e32 v115, v181, v181
	v_fmac_f32_e32 v114, v182, v182
	v_fmac_f32_e32 v115, v180, v180
	v_add_f32_e32 v114, v114, v115
	v_mul_f32_e32 v115, v129, v129
	v_mul_f32_e32 v116, v127, v127
	v_fmac_f32_e32 v115, v128, v128
	v_fmac_f32_e32 v116, v126, v126
	v_add_f32_e32 v115, v115, v116
	v_add_f32_e32 v114, v114, v115
	v_mul_f32_e32 v115, v123, v123
	v_mul_f32_e32 v116, v121, v121
	v_fmac_f32_e32 v115, v122, v122
	v_fmac_f32_e32 v116, v120, v120
	v_add_f32_e32 v115, v115, v116
	v_mul_f32_e32 v116, v125, v125
	v_mul_f32_e32 v117, v119, v119
	v_fmac_f32_e32 v116, v124, v124
	v_fmac_f32_e32 v117, v118, v118
	v_add_f32_e32 v116, v116, v117
	v_add_f32_e32 v115, v115, v116
	v_add_f32_e32 v114, v114, v115
	v_mov_b32_e32 v115, v114
	s_nop 1
	v_permlane16_swap_b32_e32 v114, v115
	s_lshl_b32 s28, s28, 2
	v_cmp_eq_u32_e64 s[6:7], 0, v191
	s_ashr_i32 s29, s28, 31
	s_waitcnt lgkmcnt(0)
	v_add_f32_e32 v114, v114, v115
	v_mov_b32_e32 v115, v114
	s_nop 1
	v_permlane32_swap_b32_e32 v114, v115
	s_and_saveexec_b64 s[30:31], s[6:7]
	s_cbranch_execz .LBB0_1315
	v_add_f32_e32 v116, v114, v115
	v_lshlrev_b64 v[114:115], 6, v[164:165]
	v_lshl_add_u64 v[114:115], s[14:15], 0, v[114:115]
	v_lshl_add_u64 v[114:115], s[28:29], 2, v[114:115]
	s_lshl_b32 s50, s64, 2
	v_lshl_add_u64 v[114:115], v[114:115], 0, s[50:51]
	s_and_b64 vcc, exec, s[16:17]
	s_cbranch_vccz .LBB0_1407
	global_store_dword v[114:115], v116, off
	s_cbranch_execnz .LBB0_1315

; __device__ __forceinline__ void st_wt4(void* p, float v) { asm volatile("global_store_dword %0, %1, off sc1" :: "v"(p), "v"(v) : "memory"); }
; template <int M> __device__ __forceinline__ float xor_add(float v) {
;     if constexpr (M < 32) return v + __int_as_float(__builtin_amdgcn_ds_swizzle(__float_as_int(v), (M << 10) | 0x1f));
;     else { auto rr = __builtin_amdgcn_permlane32_swap(__float_as_uint(v), __float_as_uint(v), false, false); return __uint_as_float(rr[0]) + __uint_as_float(rr[1]); }
;     __device__ __forceinline__ void operator()(const f32x4 (&acc)[2][2][4][2], const Unit& u, int wr, int wc, int fr, int fq) const {
;     ...
;                     ss += ((h0[0] * h0[0] + h0[1] * h0[1]) + (h0[2] * h0[2] + h0[3] * h0[3])) + ((h1[0] * h1[0] + h1[1] * h1[1]) + (h1[2] * h1[2] + h1[3] * h1[3]));
;                 }
;                 ss = xor_add<16>(ss); ss = xor_add<32>(ss);
;                 if (fq == 0) { if (WT && wt) st_wt4(ssqp + SO + (size_t)row * 16 + u.pn * 4 + wc, ss); else ssqp[SO + (size_t)row * 16 + u.pn * 4 + wc] = ss; }
.LBB0_1321:
	s_nop 0
	v_mul_f32_e32 v98, v115, v115
	v_mul_f32_e32 v99, v113, v113
	v_fmac_f32_e32 v98, v114, v114
	v_fmac_f32_e32 v99, v112, v112
	v_add_f32_e32 v98, v98, v99
	v_mul_f32_e32 v99, v117, v117
	v_mul_f32_e32 v100, v111, v111
	v_fmac_f32_e32 v99, v116, v116
	v_fmac_f32_e32 v100, v110, v110
	v_add_f32_e32 v99, v99, v100
	v_add_f32_e32 v98, v98, v99
	v_mul_f32_e32 v99, v107, v107
	v_mul_f32_e32 v100, v105, v105
	v_fmac_f32_e32 v99, v106, v106
	v_fmac_f32_e32 v100, v104, v104
	v_add_f32_e32 v99, v99, v100
	v_mul_f32_e32 v100, v109, v109
	v_mul_f32_e32 v101, v103, v103
	v_fmac_f32_e32 v100, v108, v108
	v_fmac_f32_e32 v101, v102, v102
	v_add_f32_e32 v100, v100, v101
	v_add_f32_e32 v99, v99, v100
	v_add_f32_e32 v98, v98, v99
	v_mov_b32_e32 v99, v98
	s_nop 1
	v_permlane16_swap_b32_e32 v98, v99
	s_waitcnt lgkmcnt(0)
	v_add_f32_e32 v98, v98, v99
	v_mov_b32_e32 v99, v98
	s_nop 1
	v_permlane32_swap_b32_e32 v98, v99
	s_and_saveexec_b64 s[30:31], s[6:7]
	s_cbranch_execz .LBB0_1325
	v_add_f32_e32 v100, v98, v99
	v_lshlrev_b64 v[98:99], 6, v[176:177]
	v_lshl_add_u64 v[98:99], s[14:15], 0, v[98:99]
	v_lshl_add_u64 v[98:99], s[28:29], 2, v[98:99]
	s_lshl_b32 s50, s64, 2
	s_and_b64 vcc, exec, s[4:5]
	v_lshl_add_u64 v[98:99], v[98:99], 0, s[50:51]
	s_cbranch_vccnz .LBB0_1408
	global_store_dword v[98:99], v100, off
	s_cbranch_execnz .LBB0_1325

; __device__ __forceinline__ void st_wt4(void* p, float v) { asm volatile("global_store_dword %0, %1, off sc1" :: "v"(p), "v"(v) : "memory"); }
; template <int M> __device__ __forceinline__ float xor_add(float v) {
;     if constexpr (M < 32) return v + __int_as_float(__builtin_amdgcn_ds_swizzle(__float_as_int(v), (M << 10) | 0x1f));
;     else { auto rr = __builtin_amdgcn_permlane32_swap(__float_as_uint(v), __float_as_uint(v), false, false); return __uint_as_float(rr[0]) + __uint_as_float(rr[1]); }
;     __device__ __forceinline__ void operator()(const f32x4 (&acc)[2][2][4][2], const Unit& u, int wr, int wc, int fr, int fq) const {
;     ...
;                     ss += ((h0[0] * h0[0] + h0[1] * h0[1]) + (h0[2] * h0[2] + h0[3] * h0[3])) + ((h1[0] * h1[0] + h1[1] * h1[1]) + (h1[2] * h1[2] + h1[3] * h1[3]));
;                 }
;                 ss = xor_add<16>(ss); ss = xor_add<32>(ss);
;                 if (fq == 0) { if (WT && wt) st_wt4(ssqp + SO + (size_t)row * 16 + u.pn * 4 + wc, ss); else ssqp[SO + (size_t)row * 16 + u.pn * 4 + wc] = ss; }
.LBB0_1331:
	s_nop 0
	v_mul_f32_e32 v82, v99, v99
	v_mul_f32_e32 v83, v97, v97
	v_fmac_f32_e32 v82, v98, v98
	v_fmac_f32_e32 v83, v96, v96
	v_add_f32_e32 v82, v82, v83
	v_mul_f32_e32 v83, v101, v101
	v_mul_f32_e32 v84, v95, v95
	v_fmac_f32_e32 v83, v100, v100
	v_fmac_f32_e32 v84, v94, v94
	v_add_f32_e32 v83, v83, v84
	v_add_f32_e32 v82, v82, v83
	v_mul_f32_e32 v83, v91, v91
	v_mul_f32_e32 v84, v89, v89
	v_fmac_f32_e32 v83, v90, v90
	v_fmac_f32_e32 v84, v88, v88
	v_add_f32_e32 v83, v83, v84
	v_mul_f32_e32 v84, v93, v93
	v_mul_f32_e32 v85, v87, v87
	v_fmac_f32_e32 v84, v92, v92
	v_fmac_f32_e32 v85, v86, v86
	v_add_f32_e32 v84, v84, v85
	v_add_f32_e32 v83, v83, v84
	v_add_f32_e32 v82, v82, v83
	v_mov_b32_e32 v83, v82
	s_nop 1
	v_permlane16_swap_b32_e32 v82, v83
	s_waitcnt lgkmcnt(0)
	v_add_f32_e32 v82, v82, v83
	v_mov_b32_e32 v83, v82
	s_nop 1
	v_permlane32_swap_b32_e32 v82, v83
	s_and_saveexec_b64 s[30:31], s[6:7]
	s_cbranch_execz .LBB0_1335
	v_add_f32_e32 v84, v82, v83
	v_lshlrev_b64 v[82:83], 6, v[172:173]
	v_lshl_add_u64 v[82:83], s[14:15], 0, v[82:83]
	v_lshl_add_u64 v[82:83], s[28:29], 2, v[82:83]
	s_lshl_b32 s50, s64, 2
	s_and_b64 vcc, exec, s[4:5]
	v_lshl_add_u64 v[82:83], v[82:83], 0, s[50:51]
	s_cbranch_vccnz .LBB0_1409
	global_store_dword v[82:83], v84, off
	s_cbranch_execnz .LBB0_1335

; __device__ __forceinline__ void st_wt4(void* p, float v) { asm volatile("global_store_dword %0, %1, off sc1" :: "v"(p), "v"(v) : "memory"); }
; template <int M> __device__ __forceinline__ float xor_add(float v) {
;     if constexpr (M < 32) return v + __int_as_float(__builtin_amdgcn_ds_swizzle(__float_as_int(v), (M << 10) | 0x1f));
;     else { auto rr = __builtin_amdgcn_permlane32_swap(__float_as_uint(v), __float_as_uint(v), false, false); return __uint_as_float(rr[0]) + __uint_as_float(rr[1]); }
;     __device__ __forceinline__ void operator()(const f32x4 (&acc)[2][2][4][2], const Unit& u, int wr, int wc, int fr, int fq) const {
;     ...
;                     ss += ((h0[0] * h0[0] + h0[1] * h0[1]) + (h0[2] * h0[2] + h0[3] * h0[3])) + ((h1[0] * h1[0] + h1[1] * h1[1]) + (h1[2] * h1[2] + h1[3] * h1[3]));
;                 }
;                 ss = xor_add<16>(ss); ss = xor_add<32>(ss);
;                 if (fq == 0) { if (WT && wt) st_wt4(ssqp + SO + (size_t)row * 16 + u.pn * 4 + wc, ss); else ssqp[SO + (size_t)row * 16 + u.pn * 4 + wc] = ss; }
.LBB0_1341:
	s_nop 0
	v_mul_f32_e32 v66, v83, v83
	v_mul_f32_e32 v67, v81, v81
	v_fmac_f32_e32 v66, v82, v82
	v_fmac_f32_e32 v67, v80, v80
	v_add_f32_e32 v66, v66, v67
	v_mul_f32_e32 v67, v85, v85
	v_mul_f32_e32 v68, v79, v79
	v_fmac_f32_e32 v67, v84, v84
	v_fmac_f32_e32 v68, v78, v78
	v_add_f32_e32 v67, v67, v68
	v_add_f32_e32 v66, v66, v67
	v_mul_f32_e32 v67, v75, v75
	v_mul_f32_e32 v68, v73, v73
	v_fmac_f32_e32 v67, v74, v74
	v_fmac_f32_e32 v68, v72, v72
	v_add_f32_e32 v67, v67, v68
	v_mul_f32_e32 v68, v77, v77
	v_mul_f32_e32 v69, v71, v71
	v_fmac_f32_e32 v68, v76, v76
	v_fmac_f32_e32 v69, v70, v70
	v_add_f32_e32 v68, v68, v69
	v_add_f32_e32 v67, v67, v68
	v_add_f32_e32 v66, v66, v67
	v_mov_b32_e32 v67, v66
	s_nop 1
	v_permlane16_swap_b32_e32 v66, v67
	s_waitcnt lgkmcnt(0)
	v_add_f32_e32 v66, v66, v67
	v_mov_b32_e32 v67, v66
	s_nop 1
	v_permlane32_swap_b32_e32 v66, v67
	s_and_saveexec_b64 s[30:31], s[6:7]
	s_cbranch_execz .LBB0_1345
	v_add_f32_e32 v68, v66, v67
	v_lshlrev_b64 v[66:67], 6, v[168:169]
	v_lshl_add_u64 v[66:67], s[14:15], 0, v[66:67]
	v_lshl_add_u64 v[66:67], s[28:29], 2, v[66:67]
	s_lshl_b32 s50, s64, 2
	s_and_b64 vcc, exec, s[4:5]
	v_lshl_add_u64 v[66:67], v[66:67], 0, s[50:51]
	s_cbranch_vccnz .LBB0_1410
	global_store_dword v[66:67], v68, off
	s_cbranch_execnz .LBB0_1345

; __device__ __forceinline__ void st_wt4(void* p, float v) { asm volatile("global_store_dword %0, %1, off sc1" :: "v"(p), "v"(v) : "memory"); }
; template <int M> __device__ __forceinline__ float xor_add(float v) {
;     if constexpr (M < 32) return v + __int_as_float(__builtin_amdgcn_ds_swizzle(__float_as_int(v), (M << 10) | 0x1f));
;     else { auto rr = __builtin_amdgcn_permlane32_swap(__float_as_uint(v), __float_as_uint(v), false, false); return __uint_as_float(rr[0]) + __uint_as_float(rr[1]); }
;     __device__ __forceinline__ void operator()(const f32x4 (&acc)[2][2][4][2], const Unit& u, int wr, int wc, int fr, int fq) const {
;     ...
;                     ss += ((h0[0] * h0[0] + h0[1] * h0[1]) + (h0[2] * h0[2] + h0[3] * h0[3])) + ((h1[0] * h1[0] + h1[1] * h1[1]) + (h1[2] * h1[2] + h1[3] * h1[3]));
;                 }
;                 ss = xor_add<16>(ss); ss = xor_add<32>(ss);
;                 if (fq == 0) { if (WT && wt) st_wt4(ssqp + SO + (size_t)row * 16 + u.pn * 4 + wc, ss); else ssqp[SO + (size_t)row * 16 + u.pn * 4 + wc] = ss; }
.LBB0_1351:
	s_nop 0
	v_mul_f32_e32 v48, v111, v111
	v_mul_f32_e32 v49, v109, v109
	v_fmac_f32_e32 v48, v110, v110
	v_fmac_f32_e32 v49, v108, v108
	v_add_f32_e32 v48, v48, v49
	v_mul_f32_e32 v49, v63, v63
	v_mul_f32_e32 v50, v61, v61
	v_fmac_f32_e32 v49, v62, v62
	v_fmac_f32_e32 v50, v60, v60
	v_add_f32_e32 v49, v49, v50
	v_add_f32_e32 v48, v48, v49
	v_mul_f32_e32 v49, v57, v57
	v_mul_f32_e32 v50, v55, v55
	v_fmac_f32_e32 v49, v56, v56
	v_fmac_f32_e32 v50, v54, v54
	v_add_f32_e32 v49, v49, v50
	v_mul_f32_e32 v50, v59, v59
	v_mul_f32_e32 v51, v53, v53
	v_fmac_f32_e32 v50, v58, v58
	v_fmac_f32_e32 v51, v52, v52
	v_add_f32_e32 v50, v50, v51
	v_add_f32_e32 v49, v49, v50
	v_add_f32_e32 v48, v48, v49
	v_mov_b32_e32 v49, v48
	s_nop 1
	v_permlane16_swap_b32_e32 v48, v49
	s_waitcnt lgkmcnt(0)
	v_add_f32_e32 v48, v48, v49
	v_mov_b32_e32 v49, v48
	s_nop 1
	v_permlane32_swap_b32_e32 v48, v49
	s_and_saveexec_b64 s[30:31], s[6:7]
	s_cbranch_execz .LBB0_1355
	v_add_f32_e32 v50, v48, v49
	v_lshlrev_b64 v[48:49], 6, v[106:107]
	v_lshl_add_u64 v[48:49], s[14:15], 0, v[48:49]
	v_lshl_add_u64 v[48:49], s[28:29], 2, v[48:49]
	s_lshl_b32 s50, s64, 2
	s_and_b64 vcc, exec, s[4:5]
	v_lshl_add_u64 v[48:49], v[48:49], 0, s[50:51]
	s_cbranch_vccnz .LBB0_1411
	global_store_dword v[48:49], v50, off
	s_cbranch_execnz .LBB0_1355

; __device__ __forceinline__ void st_wt4(void* p, float v) { asm volatile("global_store_dword %0, %1, off sc1" :: "v"(p), "v"(v) : "memory"); }
; template <int M> __device__ __forceinline__ float xor_add(float v) {
;     if constexpr (M < 32) return v + __int_as_float(__builtin_amdgcn_ds_swizzle(__float_as_int(v), (M << 10) | 0x1f));
;     else { auto rr = __builtin_amdgcn_permlane32_swap(__float_as_uint(v), __float_as_uint(v), false, false); return __uint_as_float(rr[0]) + __uint_as_float(rr[1]); }
;     __device__ __forceinline__ void operator()(const f32x4 (&acc)[2][2][4][2], const Unit& u, int wr, int wc, int fr, int fq) const {
;     ...
;                     ss += ((h0[0] * h0[0] + h0[1] * h0[1]) + (h0[2] * h0[2] + h0[3] * h0[3])) + ((h1[0] * h1[0] + h1[1] * h1[1]) + (h1[2] * h1[2] + h1[3] * h1[3]));
;                 }
;                 ss = xor_add<16>(ss); ss = xor_add<32>(ss);
;                 if (fq == 0) { if (WT && wt) st_wt4(ssqp + SO + (size_t)row * 16 + u.pn * 4 + wc, ss); else ssqp[SO + (size_t)row * 16 + u.pn * 4 + wc] = ss; }
.LBB0_1361:
	s_nop 0
	v_mul_f32_e32 v32, v49, v49
	v_mul_f32_e32 v33, v39, v39
	v_fmac_f32_e32 v32, v48, v48
	v_fmac_f32_e32 v33, v38, v38
	v_add_f32_e32 v32, v32, v33
	v_mul_f32_e32 v33, v51, v51
	v_mul_f32_e32 v34, v37, v37
	v_fmac_f32_e32 v33, v50, v50
	v_fmac_f32_e32 v34, v36, v36
	v_add_f32_e32 v33, v33, v34
	v_add_f32_e32 v32, v32, v33
	v_mul_f32_e32 v33, v45, v45
	v_mul_f32_e32 v34, v47, v47
	v_fmac_f32_e32 v33, v44, v44
	v_fmac_f32_e32 v34, v46, v46
	v_add_f32_e32 v33, v33, v34
	v_mul_f32_e32 v34, v41, v41
	v_mul_f32_e32 v35, v43, v43
	v_fmac_f32_e32 v34, v40, v40
	v_fmac_f32_e32 v35, v42, v42
	v_add_f32_e32 v34, v34, v35
	v_add_f32_e32 v33, v33, v34
	v_add_f32_e32 v32, v32, v33
	v_mov_b32_e32 v33, v32
	s_nop 1
	v_permlane16_swap_b32_e32 v32, v33
	s_waitcnt lgkmcnt(0)
	v_add_f32_e32 v32, v32, v33
	v_mov_b32_e32 v33, v32
	s_nop 1
	v_permlane32_swap_b32_e32 v32, v33
	s_and_saveexec_b64 s[30:31], s[6:7]
	s_cbranch_execz .LBB0_1365
	v_add_f32_e32 v34, v32, v33
	v_lshlrev_b64 v[32:33], 6, v[102:103]
	v_lshl_add_u64 v[32:33], s[14:15], 0, v[32:33]
	v_lshl_add_u64 v[32:33], s[28:29], 2, v[32:33]
	s_lshl_b32 s50, s64, 2
	s_and_b64 vcc, exec, s[4:5]
	v_lshl_add_u64 v[32:33], v[32:33], 0, s[50:51]
	s_cbranch_vccnz .LBB0_1412
	global_store_dword v[32:33], v34, off
	s_cbranch_execnz .LBB0_1365

; __device__ __forceinline__ void st_wt4(void* p, float v) { asm volatile("global_store_dword %0, %1, off sc1" :: "v"(p), "v"(v) : "memory"); }
; template <int M> __device__ __forceinline__ float xor_add(float v) {
;     if constexpr (M < 32) return v + __int_as_float(__builtin_amdgcn_ds_swizzle(__float_as_int(v), (M << 10) | 0x1f));
;     else { auto rr = __builtin_amdgcn_permlane32_swap(__float_as_uint(v), __float_as_uint(v), false, false); return __uint_as_float(rr[0]) + __uint_as_float(rr[1]); }
;     __device__ __forceinline__ void operator()(const f32x4 (&acc)[2][2][4][2], const Unit& u, int wr, int wc, int fr, int fq) const {
;     ...
;                     ss += ((h0[0] * h0[0] + h0[1] * h0[1]) + (h0[2] * h0[2] + h0[3] * h0[3])) + ((h1[0] * h1[0] + h1[1] * h1[1]) + (h1[2] * h1[2] + h1[3] * h1[3]));
;                 }
;                 ss = xor_add<16>(ss); ss = xor_add<32>(ss);
;                 if (fq == 0) { if (WT && wt) st_wt4(ssqp + SO + (size_t)row * 16 + u.pn * 4 + wc, ss); else ssqp[SO + (size_t)row * 16 + u.pn * 4 + wc] = ss; }
.LBB0_1371:
	s_nop 0
	v_mul_f32_e32 v16, v33, v33
	v_mul_f32_e32 v17, v23, v23
	v_fmac_f32_e32 v16, v32, v32
	v_fmac_f32_e32 v17, v22, v22
	v_add_f32_e32 v16, v16, v17
	v_mul_f32_e32 v17, v35, v35
	v_mul_f32_e32 v18, v21, v21
	v_fmac_f32_e32 v17, v34, v34
	v_fmac_f32_e32 v18, v20, v20
	v_add_f32_e32 v17, v17, v18
	v_add_f32_e32 v16, v16, v17
	v_mul_f32_e32 v17, v29, v29
	v_mul_f32_e32 v18, v31, v31
	v_fmac_f32_e32 v17, v28, v28
	v_fmac_f32_e32 v18, v30, v30
	v_add_f32_e32 v17, v17, v18
	v_mul_f32_e32 v18, v25, v25
	v_mul_f32_e32 v19, v27, v27
	v_fmac_f32_e32 v18, v24, v24
	v_fmac_f32_e32 v19, v26, v26
	v_add_f32_e32 v18, v18, v19
	v_add_f32_e32 v17, v17, v18
	v_add_f32_e32 v16, v16, v17
	v_mov_b32_e32 v17, v16
	s_nop 1
	v_permlane16_swap_b32_e32 v16, v17
	s_waitcnt lgkmcnt(0)
	v_add_f32_e32 v16, v16, v17
	v_mov_b32_e32 v17, v16
	s_nop 1
	v_permlane32_swap_b32_e32 v16, v17
	s_and_saveexec_b64 s[30:31], s[6:7]
	s_cbranch_execz .LBB0_1375
	v_add_f32_e32 v18, v16, v17
	v_lshlrev_b64 v[16:17], 6, v[98:99]
	v_lshl_add_u64 v[16:17], s[14:15], 0, v[16:17]
	v_lshl_add_u64 v[16:17], s[28:29], 2, v[16:17]
	s_lshl_b32 s50, s64, 2
	s_and_b64 vcc, exec, s[4:5]
	v_lshl_add_u64 v[16:17], v[16:17], 0, s[50:51]
	s_cbranch_vccnz .LBB0_1413
	global_store_dword v[16:17], v18, off
	s_cbranch_execnz .LBB0_1375

; __device__ __forceinline__ void st_wt4(void* p, float v) { asm volatile("global_store_dword %0, %1, off sc1" :: "v"(p), "v"(v) : "memory"); }
; template <int M> __device__ __forceinline__ float xor_add(float v) {
;     if constexpr (M < 32) return v + __int_as_float(__builtin_amdgcn_ds_swizzle(__float_as_int(v), (M << 10) | 0x1f));
;     else { auto rr = __builtin_amdgcn_permlane32_swap(__float_as_uint(v), __float_as_uint(v), false, false); return __uint_as_float(rr[0]) + __uint_as_float(rr[1]); }
;     __device__ __forceinline__ void operator()(const f32x4 (&acc)[2][2][4][2], const Unit& u, int wr, int wc, int fr, int fq) const {
;     ...
;                     ss += ((h0[0] * h0[0] + h0[1] * h0[1]) + (h0[2] * h0[2] + h0[3] * h0[3])) + ((h1[0] * h1[0] + h1[1] * h1[1]) + (h1[2] * h1[2] + h1[3] * h1[3]));
;                 }
;                 ss = xor_add<16>(ss); ss = xor_add<32>(ss);
;                 if (fq == 0) { if (WT && wt) st_wt4(ssqp + SO + (size_t)row * 16 + u.pn * 4 + wc, ss); else ssqp[SO + (size_t)row * 16 + u.pn * 4 + wc] = ss; }
.LBB0_1381:
	s_nop 0
	v_mul_f32_e32 v0, v17, v17
	v_mul_f32_e32 v1, v7, v7
	v_fmac_f32_e32 v0, v16, v16
	v_fmac_f32_e32 v1, v6, v6
	v_add_f32_e32 v0, v0, v1
	v_mul_f32_e32 v1, v19, v19
	v_mul_f32_e32 v2, v5, v5
	v_fmac_f32_e32 v1, v18, v18
	v_fmac_f32_e32 v2, v4, v4
	v_add_f32_e32 v1, v1, v2
	v_add_f32_e32 v0, v0, v1
	v_mul_f32_e32 v1, v13, v13
	v_mul_f32_e32 v2, v15, v15
	v_fmac_f32_e32 v1, v12, v12
	v_fmac_f32_e32 v2, v14, v14
	v_add_f32_e32 v1, v1, v2
	v_mul_f32_e32 v2, v9, v9
	v_mul_f32_e32 v3, v11, v11
	v_fmac_f32_e32 v2, v8, v8
	v_fmac_f32_e32 v3, v10, v10
	v_add_f32_e32 v2, v2, v3
	v_add_f32_e32 v1, v1, v2
	v_add_f32_e32 v0, v0, v1
	v_mov_b32_e32 v1, v0
	s_nop 1
	v_permlane16_swap_b32_e32 v0, v1
	s_waitcnt lgkmcnt(0)
	v_add_f32_e32 v0, v0, v1
	v_mov_b32_e32 v1, v0
	s_nop 1
	v_permlane32_swap_b32_e32 v0, v1
	s_and_saveexec_b64 s[30:31], s[6:7]
	s_cbranch_execz .LBB0_1385
	v_add_f32_e32 v2, v0, v1
	v_lshlrev_b64 v[0:1], 6, v[94:95]
	v_lshl_add_u64 v[0:1], s[14:15], 0, v[0:1]
	v_lshl_add_u64 v[0:1], s[28:29], 2, v[0:1]
	s_lshl_b32 s50, s64, 2
	s_and_b64 vcc, exec, s[4:5]
	v_lshl_add_u64 v[0:1], v[0:1], 0, s[50:51]
	s_cbranch_vccnz .LBB0_1414
	global_store_dword v[0:1], v2, off
	s_cbranch_execnz .LBB0_1385
